# nt cache hint also on the prologue's f32 x and memory-token loads, the layer-0 residual x loads and the final f32 output stores
# speedup vs baseline: 1.0268x; 1.0106x over previous
; template <int PH, bool PRB = false>
; __device__ __forceinline__ void run_phase(int layer, LAS unsigned char* lds, const int wv_) {
;     ...
;         for (int r = gw; r < S; r += NGW) {
;             const float4* s4 = (const float4*)(p.x + (size_t)r * D); float4 v[4]; float ss = 0.f;
; #pragma unroll
;             for (int j = 0; j < 4; ++j) { v[j] = s4[lane + 64 * j]; ss += v[j].x * v[j].x + v[j].y * v[j].y + v[j].z * v[j].z + v[j].w * v[j].w; }
;             ss = wave_sum(ss);
;             rms_row_bf16(v, 1.0f, nullptr, hb + (size_t)r * D, lane);
;             if (lane < 16) ssqp[(size_t)r * 16 + lane] = lane == 0 ? ss : 0.f;
;             if (lane == 0) ((float*)(ws + WS_MISC + MISC_RSROW))[r] = rsqrtf(ss * (1.0f / D) + 1e-6f);
.LBB0_41:
	global_load_dwordx4 v[12:15], v[10:11], off nt
	global_load_dwordx4 v[16:19], v[10:11], off offset:1024 nt
	global_load_dwordx4 v[20:23], v[10:11], off offset:2048 nt
	global_load_dwordx4 v[24:27], v[10:11], off offset:3072 nt
	s_waitcnt vmcnt(3)
	v_mul_f32_e32 v4, v13, v13
	s_waitcnt vmcnt(2)
	v_mul_f32_e32 v28, v17, v17
	s_waitcnt vmcnt(1)
	v_mul_f32_e32 v29, v21, v21
	v_fmac_f32_e32 v4, v12, v12
	v_fmac_f32_e32 v28, v16, v16
	s_waitcnt vmcnt(0)
	v_mul_f32_e32 v30, v25, v25
	v_fmac_f32_e32 v29, v20, v20
	v_fmac_f32_e32 v4, v14, v14
	v_fmac_f32_e32 v28, v18, v18
	v_fmac_f32_e32 v30, v24, v24
	v_fmac_f32_e32 v29, v22, v22
	v_fmac_f32_e32 v4, v15, v15
	v_fmac_f32_e32 v28, v19, v19
	v_fmac_f32_e32 v30, v26, v26
	v_fmac_f32_e32 v29, v23, v23
	v_add_f32_e32 v4, v4, v28
	v_fmac_f32_e32 v30, v27, v27
	v_add_f32_e32 v4, v4, v29
	v_add_f32_e32 v4, v4, v30
	ds_swizzle_b32 v28, v4 offset:swizzle(SWAP,1)
	v_cvt_pk_bf16_f32 v12, v12, v13
	v_cvt_pk_bf16_f32 v13, v14, v15
	s_waitcnt lgkmcnt(0)
	v_add_f32_e32 v4, v4, v28
	ds_swizzle_b32 v30, v4 offset:swizzle(SWAP,2)
	v_lshl_add_u64 v[28:29], s[44:45], 0, v[8:9]
	v_add_co_u32_e64 v28, s[6:7], s25, v28
	s_waitcnt lgkmcnt(0)
	v_add_f32_e32 v4, v4, v30
	ds_swizzle_b32 v30, v4 offset:swizzle(SWAP,4)
	v_addc_co_u32_e64 v29, s[6:7], 0, v29, s[6:7]
	global_store_dwordx2 v[28:29], v[12:13], off
	v_cvt_pk_bf16_f32 v12, v16, v17
	s_waitcnt lgkmcnt(0)
	v_add_f32_e32 v4, v4, v30
	ds_swizzle_b32 v14, v4 offset:swizzle(SWAP,8)
	v_cvt_pk_bf16_f32 v13, v18, v19
	global_store_dwordx2 v[28:29], v[12:13], off offset:512
	v_cvt_pk_bf16_f32 v12, v20, v21
	v_cvt_pk_bf16_f32 v13, v22, v23
	s_waitcnt lgkmcnt(0)
	v_add_f32_e32 v4, v4, v14
	ds_swizzle_b32 v14, v4 offset:swizzle(SWAP,16)
	global_store_dwordx2 v[28:29], v[12:13], off offset:1024
	v_cvt_pk_bf16_f32 v12, v24, v25
	v_cvt_pk_bf16_f32 v13, v26, v27
	global_store_dwordx2 v[28:29], v[12:13], off offset:1536
	s_waitcnt lgkmcnt(0)
	v_add_f32_e32 v4, v4, v14
	v_mov_b32_e32 v14, v4
	s_nop 1
	v_permlane32_swap_b32_e32 v4, v14
	v_add_f32_e32 v4, v4, v14
	s_and_saveexec_b64 s[6:7], vcc
	s_cbranch_execz .LBB0_43
	v_cndmask_b32_e64 v14, 0, v4, s[4:5]
	v_lshl_add_u64 v[12:13], s[44:45], 0, v[6:7]
	global_store_dword v[12:13], v14, off

; __device__ __forceinline__ unsigned cvt_pk_bf16(float lo, float hi) { unsigned r; asm volatile("v_cvt_pk_bf16_f32 %0, %1, %2" : "=v"(r) : "v"(lo), "v"(hi)); return r; }
; __device__ __forceinline__ void rms_row_bf16(const float4 (&v)[4], float rs, const float* g, bf16* dst, int lane) {
; #pragma unroll
;     for (int j = 0; j < 4; ++j) { const float4 gg = g ? ((const float4*)g)[lane + 64 * j] : make_float4(1.f, 1.f, 1.f, 1.f);
;         u32x2 w; w.x = cvt_pk_bf16(v[j].x * rs * gg.x, v[j].y * rs * gg.y); w.y = cvt_pk_bf16(v[j].z * rs * gg.z, v[j].w * rs * gg.w); ((u32x2*)dst)[lane + 64 * j] = w; }
; template <int PH, bool PRB = false>
; __device__ __forceinline__ void run_phase(int layer, LAS unsigned char* lds, const int wv_) {
;     ...
;         for (int r = gw; r < MEM; r += NGW) {
;             const float4* s4 = (const float4*)(p.mem + (size_t)r * D); float4 v[4]; float ss = 0.f;
; #pragma unroll
;             for (int j = 0; j < 4; ++j) { v[j] = s4[lane + 64 * j]; ss += v[j].x * v[j].x + v[j].y * v[j].y + v[j].z * v[j].z + v[j].w * v[j].w; }
;             const float rs = rsqrtf(wave_sum(ss) * (1.0f / D) + 1e-6f);
;             for (int l = 0; l < DEPTH; ++l) rms_row_bf16(v, rs, p.ln_mem + l * D, memn + ((size_t)l * MEM + r) * D, lane);
.LBB0_48:
	global_load_dwordx4 v[14:17], v[54:55], off nt
	global_load_dwordx4 v[10:13], v[54:55], off offset:1024 nt
	global_load_dwordx4 v[6:9], v[54:55], off offset:2048 nt
	global_load_dwordx4 v[2:5], v[54:55], off offset:3072 nt
	s_and_b64 vcc, exec, s[4:5]
	v_mov_b32_e32 v22, 1.0
	v_mov_b32_e32 v23, 1.0
	s_waitcnt vmcnt(3)
	v_mul_f32_e32 v18, v15, v15
	s_waitcnt vmcnt(2)
	v_mul_f32_e32 v19, v11, v11
	s_waitcnt vmcnt(1)
	v_mul_f32_e32 v20, v7, v7
	v_fmac_f32_e32 v18, v14, v14
	v_fmac_f32_e32 v19, v10, v10
	s_waitcnt vmcnt(0)
	v_mul_f32_e32 v21, v3, v3
	v_fmac_f32_e32 v20, v6, v6
	v_fmac_f32_e32 v18, v16, v16
	v_fmac_f32_e32 v19, v12, v12
	v_fmac_f32_e32 v21, v2, v2
	v_fmac_f32_e32 v20, v8, v8
	v_fmac_f32_e32 v18, v17, v17
	v_fmac_f32_e32 v19, v13, v13
	v_fmac_f32_e32 v21, v4, v4
	v_fmac_f32_e32 v20, v9, v9
	v_add_f32_e32 v18, v18, v19
	v_fmac_f32_e32 v21, v5, v5
	v_add_f32_e32 v18, v18, v20
	v_add_f32_e32 v18, v18, v21
	ds_swizzle_b32 v19, v18 offset:swizzle(SWAP,1)
	s_waitcnt lgkmcnt(0)
	v_add_f32_e32 v18, v18, v19
	ds_swizzle_b32 v19, v18 offset:swizzle(SWAP,2)
	s_waitcnt lgkmcnt(0)
	v_add_f32_e32 v18, v18, v19
	ds_swizzle_b32 v19, v18 offset:swizzle(SWAP,4)
	s_waitcnt lgkmcnt(0)
	v_add_f32_e32 v19, v18, v19
	ds_swizzle_b32 v20, v19 offset:swizzle(SWAP,8)
	v_mov_b32_e32 v18, 1.0
	s_waitcnt lgkmcnt(0)
	v_add_f32_e32 v19, v19, v20
	ds_swizzle_b32 v21, v19 offset:swizzle(SWAP,16)
	v_mov_b32_e32 v20, 1.0
	s_waitcnt lgkmcnt(0)
	v_add_f32_e32 v19, v19, v21
	v_mov_b32_e32 v57, v19
	s_nop 1
	v_permlane32_swap_b32_e32 v19, v57
	v_mov_b32_e32 v21, 1.0
	s_cbranch_vccnz .LBB0_50
	global_load_dwordx4 v[20:23], v[24:25], off nt
.LBB0_50:
	v_add_f32_e32 v19, v19, v57
	v_fmamk_f32 v19, v19, 0x3a800000, v35
	v_mul_f32_e32 v57, 0x4b800000, v19
	v_cmp_gt_f32_e32 vcc, s8, v19
	s_nop 1
	v_cndmask_b32_e32 v19, v19, v57, vcc
	v_rsq_f32_e32 v19, v19
	s_nop 0
	v_mul_f32_e32 v57, 0x45800000, v19
	v_cndmask_b32_e32 v61, v19, v57, vcc
	v_mul_f32_e32 v60, v14, v61
	v_mul_f32_e32 v59, v15, v61
	v_mul_f32_e32 v57, v16, v61
	v_mul_f32_e32 v58, v17, v61
	s_waitcnt vmcnt(0)
	v_mul_f32_e32 v14, v60, v20
	v_mul_f32_e32 v15, v59, v21
	v_cvt_pk_bf16_f32 v14, v14, v15
	v_mul_f32_e32 v15, v57, v22
	v_mul_f32_e32 v16, v58, v23
	v_cvt_pk_bf16_f32 v15, v15, v16
	v_add_co_u32_e32 v16, vcc, 0xffe80000, v52
	v_mov_b32_e32 v19, 1.0
	s_nop 0
	v_addc_co_u32_e32 v17, vcc, -1, v53, vcc
	global_store_dwordx2 v[16:17], v[14:15], off offset:-1536
	s_and_b64 vcc, exec, s[4:5]
	v_mov_b32_e32 v16, 1.0
	v_mov_b32_e32 v17, 1.0
	s_cbranch_vccnz .LBB0_52
	global_load_dwordx4 v[16:19], v[24:25], off offset:1024 nt
.LBB0_52:
	v_mul_f32_e32 v23, v10, v61
	v_mul_f32_e32 v22, v11, v61
	v_mul_f32_e32 v20, v12, v61
	v_mul_f32_e32 v21, v13, v61
	s_waitcnt vmcnt(0)
	v_mul_f32_e32 v10, v23, v16
	v_mul_f32_e32 v11, v22, v17
	v_cvt_pk_bf16_f32 v10, v10, v11
	v_mul_f32_e32 v11, v20, v18
	v_mul_f32_e32 v12, v21, v19
	v_cvt_pk_bf16_f32 v11, v11, v12
	v_add_co_u32_e32 v12, vcc, 0xffe80000, v52
	v_mov_b32_e32 v14, 1.0
	s_nop 0
	v_addc_co_u32_e32 v13, vcc, -1, v53, vcc
	global_store_dwordx2 v[12:13], v[10:11], off offset:-1024
	v_mov_b32_e32 v10, 1.0
	s_and_b64 vcc, exec, s[4:5]
	v_mov_b32_e32 v15, 1.0
	v_mov_b32_e32 v12, 1.0
	v_mov_b32_e32 v13, 1.0
	s_cbranch_vccnz .LBB0_54
	global_load_dwordx4 v[12:15], v[24:25], off offset:2048 nt
.LBB0_54:
	v_mul_f32_e32 v19, v6, v61
	v_mul_f32_e32 v18, v7, v61
	v_mul_f32_e32 v16, v8, v61
	v_mul_f32_e32 v17, v9, v61
	s_waitcnt vmcnt(0)
	v_mul_f32_e32 v6, v19, v12
	v_mul_f32_e32 v7, v18, v13
	v_cvt_pk_bf16_f32 v6, v6, v7
	v_mul_f32_e32 v7, v16, v14
	v_mul_f32_e32 v8, v17, v15
	v_cvt_pk_bf16_f32 v7, v7, v8
	v_add_co_u32_e32 v8, vcc, 0xffe80000, v52
	v_mov_b32_e32 v11, 1.0
	s_nop 0
	v_addc_co_u32_e32 v9, vcc, -1, v53, vcc
	global_store_dwordx2 v[8:9], v[6:7], off offset:-512
	s_and_b64 vcc, exec, s[4:5]
	v_mov_b32_e32 v8, 1.0
	v_mov_b32_e32 v9, 1.0
	s_cbranch_vccnz .LBB0_56
	global_load_dwordx4 v[8:11], v[24:25], off offset:3072 nt
.LBB0_56:
	v_mul_f32_e32 v15, v2, v61
	v_mul_f32_e32 v14, v3, v61
	v_mul_f32_e32 v12, v4, v61
	v_mul_f32_e32 v13, v5, v61
	s_waitcnt vmcnt(0)
	v_mul_f32_e32 v2, v15, v8
	v_mul_f32_e32 v3, v14, v9
	v_cvt_pk_bf16_f32 v2, v2, v3
	v_mul_f32_e32 v3, v12, v10
	v_mul_f32_e32 v4, v13, v11
	v_cvt_pk_bf16_f32 v3, v3, v4
	v_add_co_u32_e32 v4, vcc, 0xffe80000, v52
	v_mov_b32_e32 v8, 1.0
	s_nop 0
	v_addc_co_u32_e32 v5, vcc, -1, v53, vcc
	global_store_dwordx2 v[4:5], v[2:3], off
	v_mov_b32_e32 v4, 1.0
	s_and_b64 vcc, exec, s[4:5]
	v_mov_b32_e32 v9, 1.0
	v_mov_b32_e32 v6, 1.0
	v_mov_b32_e32 v7, 1.0
	s_cbranch_vccnz .LBB0_58
	global_load_dwordx4 v[6:9], v[26:27], off nt
.LBB0_58:
	s_waitcnt vmcnt(0)
	v_mul_f32_e32 v2, v60, v6
	v_mul_f32_e32 v3, v59, v7
	v_cvt_pk_bf16_f32 v2, v2, v3
	v_mul_f32_e32 v3, v57, v8
	v_add_co_u32_e32 v6, vcc, 0xfff00000, v52
	v_mul_f32_e32 v5, v58, v9
	v_cvt_pk_bf16_f32 v3, v3, v5
	s_nop 0
	v_addc_co_u32_e32 v7, vcc, -1, v53, vcc
	global_store_dwordx2 v[6:7], v[2:3], off offset:-1536
	s_and_b64 vcc, exec, s[4:5]
	v_mov_b32_e32 v5, 1.0
	v_mov_b32_e32 v2, 1.0
	v_mov_b32_e32 v3, 1.0
	s_cbranch_vccnz .LBB0_60
	global_load_dwordx4 v[2:5], v[28:29], off nt
; __device__ __forceinline__ unsigned cvt_pk_bf16(float lo, float hi) { unsigned r; asm volatile("v_cvt_pk_bf16_f32 %0, %1, %2" : "=v"(r) : "v"(lo), "v"(hi)); return r; }
; __device__ __forceinline__ void rms_row_bf16(const float4 (&v)[4], float rs, const float* g, bf16* dst, int lane) {
; #pragma unroll
;     for (int j = 0; j < 4; ++j) { const float4 gg = g ? ((const float4*)g)[lane + 64 * j] : make_float4(1.f, 1.f, 1.f, 1.f);
;         u32x2 w; w.x = cvt_pk_bf16(v[j].x * rs * gg.x, v[j].y * rs * gg.y); w.y = cvt_pk_bf16(v[j].z * rs * gg.z, v[j].w * rs * gg.w); ((u32x2*)dst)[lane + 64 * j] = w; }
; template <int PH, bool PRB = false>
; __device__ __forceinline__ void run_phase(int layer, LAS unsigned char* lds, const int wv_) {
;     ...
;         for (int r = gw; r < MEM; r += NGW) {
;             const float4* s4 = (const float4*)(p.mem + (size_t)r * D); float4 v[4]; float ss = 0.f;
; #pragma unroll
;             for (int j = 0; j < 4; ++j) { v[j] = s4[lane + 64 * j]; ss += v[j].x * v[j].x + v[j].y * v[j].y + v[j].z * v[j].z + v[j].w * v[j].w; }
;             const float rs = rsqrtf(wave_sum(ss) * (1.0f / D) + 1e-6f);
;             for (int l = 0; l < DEPTH; ++l) rms_row_bf16(v, rs, p.ln_mem + l * D, memn + ((size_t)l * MEM + r) * D, lane);
.LBB0_60:
	s_waitcnt vmcnt(0)
	v_mul_f32_e32 v2, v23, v2
	v_mul_f32_e32 v3, v22, v3
	v_cvt_pk_bf16_f32 v2, v2, v3
	v_mul_f32_e32 v3, v20, v4
	v_mul_f32_e32 v4, v21, v5
	v_cvt_pk_bf16_f32 v3, v3, v4
	v_add_co_u32_e32 v4, vcc, 0xfff00000, v52
	v_mov_b32_e32 v8, 1.0
	s_nop 0
	v_addc_co_u32_e32 v5, vcc, -1, v53, vcc
	global_store_dwordx2 v[4:5], v[2:3], off offset:-1024
	v_mov_b32_e32 v4, 1.0
	s_and_b64 vcc, exec, s[4:5]
	v_mov_b32_e32 v9, 1.0
	v_mov_b32_e32 v6, 1.0
	v_mov_b32_e32 v7, 1.0
	s_cbranch_vccnz .LBB0_62
	global_load_dwordx4 v[6:9], v[30:31], off nt
.LBB0_62:
	s_waitcnt vmcnt(0)
	v_mul_f32_e32 v2, v19, v6
	v_mul_f32_e32 v3, v18, v7
	v_cvt_pk_bf16_f32 v2, v2, v3
	v_mul_f32_e32 v3, v16, v8
	v_add_co_u32_e32 v6, vcc, 0xfff00000, v52
	v_mul_f32_e32 v5, v17, v9
	v_cvt_pk_bf16_f32 v3, v3, v5
	s_nop 0
	v_addc_co_u32_e32 v7, vcc, -1, v53, vcc
	global_store_dwordx2 v[6:7], v[2:3], off offset:-512
	s_and_b64 vcc, exec, s[4:5]
	v_mov_b32_e32 v5, 1.0
	v_mov_b32_e32 v2, 1.0
	v_mov_b32_e32 v3, 1.0
	s_cbranch_vccnz .LBB0_64
	global_load_dwordx4 v[2:5], v[32:33], off nt
.LBB0_64:
	s_waitcnt vmcnt(0)
	v_mul_f32_e32 v2, v15, v2
	v_mul_f32_e32 v3, v14, v3
	v_cvt_pk_bf16_f32 v2, v2, v3
	v_mul_f32_e32 v3, v12, v4
	v_mul_f32_e32 v4, v13, v5
	v_cvt_pk_bf16_f32 v3, v3, v4
	v_add_co_u32_e32 v4, vcc, 0xfff00000, v52
	v_mov_b32_e32 v8, 1.0
	s_nop 0
	v_addc_co_u32_e32 v5, vcc, -1, v53, vcc
	global_store_dwordx2 v[4:5], v[2:3], off
	v_mov_b32_e32 v4, 1.0
	s_and_b64 vcc, exec, s[4:5]
	v_mov_b32_e32 v9, 1.0
	v_mov_b32_e32 v6, 1.0
	v_mov_b32_e32 v7, 1.0
	s_cbranch_vccnz .LBB0_66
	global_load_dwordx4 v[6:9], v[36:37], off nt
.LBB0_66:
	s_waitcnt vmcnt(0)
	v_mul_f32_e32 v2, v60, v6
	v_mul_f32_e32 v3, v59, v7
	v_cvt_pk_bf16_f32 v2, v2, v3
	v_mul_f32_e32 v3, v57, v8
	v_add_co_u32_e32 v6, vcc, 0xfff80000, v52
	v_mul_f32_e32 v5, v58, v9
	v_cvt_pk_bf16_f32 v3, v3, v5
	s_nop 0
	v_addc_co_u32_e32 v7, vcc, -1, v53, vcc
	global_store_dwordx2 v[6:7], v[2:3], off offset:-1536
	s_and_b64 vcc, exec, s[4:5]
	v_mov_b32_e32 v5, 1.0
	v_mov_b32_e32 v2, 1.0
	v_mov_b32_e32 v3, 1.0
	s_cbranch_vccnz .LBB0_68
	global_load_dwordx4 v[2:5], v[38:39], off nt
.LBB0_68:
	s_waitcnt vmcnt(0)
	v_mul_f32_e32 v2, v23, v2
	v_mul_f32_e32 v3, v22, v3
	v_cvt_pk_bf16_f32 v2, v2, v3
	v_mul_f32_e32 v3, v20, v4
	v_mul_f32_e32 v4, v21, v5
	v_cvt_pk_bf16_f32 v3, v3, v4
	v_add_co_u32_e32 v4, vcc, 0xfff80000, v52
	v_mov_b32_e32 v8, 1.0
	s_nop 0
	v_addc_co_u32_e32 v5, vcc, -1, v53, vcc
	global_store_dwordx2 v[4:5], v[2:3], off offset:-1024
	v_mov_b32_e32 v4, 1.0
	s_and_b64 vcc, exec, s[4:5]
	v_mov_b32_e32 v9, 1.0
	v_mov_b32_e32 v6, 1.0
	v_mov_b32_e32 v7, 1.0
	s_cbranch_vccnz .LBB0_70
	global_load_dwordx4 v[6:9], v[40:41], off nt
.LBB0_70:
	s_waitcnt vmcnt(0)
	v_mul_f32_e32 v2, v19, v6
	v_mul_f32_e32 v3, v18, v7
	v_cvt_pk_bf16_f32 v2, v2, v3
	v_mul_f32_e32 v3, v16, v8
	v_add_co_u32_e32 v6, vcc, 0xfff80000, v52
	v_mul_f32_e32 v5, v17, v9
	v_cvt_pk_bf16_f32 v3, v3, v5
	s_nop 0
	v_addc_co_u32_e32 v7, vcc, -1, v53, vcc
	global_store_dwordx2 v[6:7], v[2:3], off offset:-512
	s_and_b64 vcc, exec, s[4:5]
	v_mov_b32_e32 v5, 1.0
	v_mov_b32_e32 v2, 1.0
	v_mov_b32_e32 v3, 1.0
	s_cbranch_vccnz .LBB0_72
	global_load_dwordx4 v[2:5], v[42:43], off nt
.LBB0_72:
	s_waitcnt vmcnt(0)
	v_mul_f32_e32 v2, v15, v2
	v_mul_f32_e32 v3, v14, v3
	v_cvt_pk_bf16_f32 v2, v2, v3
	v_mul_f32_e32 v3, v12, v4
	v_mul_f32_e32 v4, v13, v5
	v_cvt_pk_bf16_f32 v3, v3, v4
	v_add_co_u32_e32 v4, vcc, 0xfff80000, v52
	v_mov_b32_e32 v8, 1.0
	s_nop 0
	v_addc_co_u32_e32 v5, vcc, -1, v53, vcc
	global_store_dwordx2 v[4:5], v[2:3], off
	v_mov_b32_e32 v4, 1.0
	s_and_b64 vcc, exec, s[4:5]
	v_mov_b32_e32 v9, 1.0
	v_mov_b32_e32 v6, 1.0
	v_mov_b32_e32 v7, 1.0
	s_cbranch_vccnz .LBB0_74
	global_load_dwordx4 v[6:9], v[44:45], off nt
.LBB0_74:
	s_waitcnt vmcnt(0)
	v_mul_f32_e32 v2, v60, v6
	v_mul_f32_e32 v3, v59, v7
	v_cvt_pk_bf16_f32 v2, v2, v3
	v_mul_f32_e32 v3, v57, v8
	v_mul_f32_e32 v5, v58, v9
	v_cvt_pk_bf16_f32 v3, v3, v5
	global_store_dwordx2 v[52:53], v[2:3], off offset:-1536
	s_and_b64 vcc, exec, s[4:5]
	v_mov_b32_e32 v5, 1.0
	v_mov_b32_e32 v2, 1.0
	v_mov_b32_e32 v3, 1.0
	s_cbranch_vccnz .LBB0_76
	global_load_dwordx4 v[2:5], v[46:47], off nt
.LBB0_76:
	s_waitcnt vmcnt(0)
	v_mul_f32_e32 v2, v23, v2
	v_mul_f32_e32 v3, v22, v3
	v_cvt_pk_bf16_f32 v2, v2, v3
	v_mul_f32_e32 v3, v20, v4
	v_mul_f32_e32 v4, v21, v5
	v_cvt_pk_bf16_f32 v3, v3, v4
	v_mov_b32_e32 v4, 1.0
	s_and_b64 vcc, exec, s[4:5]
	v_mov_b32_e32 v8, 1.0
	v_mov_b32_e32 v9, 1.0
	v_mov_b32_e32 v6, 1.0
	v_mov_b32_e32 v7, 1.0
	global_store_dwordx2 v[52:53], v[2:3], off offset:-1024
	s_cbranch_vccnz .LBB0_78
	global_load_dwordx4 v[6:9], v[48:49], off nt
.LBB0_78:
	s_waitcnt vmcnt(0)
	v_mul_f32_e32 v2, v19, v6
	v_mul_f32_e32 v3, v18, v7
	v_cvt_pk_bf16_f32 v2, v2, v3
	v_mul_f32_e32 v3, v16, v8
	v_mul_f32_e32 v5, v17, v9
	v_cvt_pk_bf16_f32 v3, v3, v5
	global_store_dwordx2 v[52:53], v[2:3], off offset:-512
	s_and_b64 vcc, exec, s[4:5]
	v_mov_b32_e32 v5, 1.0
	v_mov_b32_e32 v2, 1.0
	v_mov_b32_e32 v3, 1.0
	s_cbranch_vccnz .LBB0_47
	global_load_dwordx4 v[2:5], v[50:51], off nt
	s_branch .LBB0_47

; __device__ __forceinline__ unsigned cvt_pk_bf16(float lo, float hi) { unsigned r; asm volatile("v_cvt_pk_bf16_f32 %0, %1, %2" : "=v"(r) : "v"(lo), "v"(hi)); return r; }
; __device__ __forceinline__ void st_wt16(void* p, u32x4 v) { asm volatile("global_store_dwordx4 %0, %1, off sc1\n\ts_nop 1" :: "v"(p), "v"(v) : "memory"); }
;     __device__ __forceinline__ void operator()(const f32x4 (&acc)[2][2][4][2], const Unit& u, int wr, int wc, int fr, int fq) const {
;         const int row0 = u.pm * BM + wr * 64 + fr, col0 = u.pn * BM + wc * 32 + 8 * fq;
; #pragma unroll
;         for (int ai = 0; ai < 2; ++ai) {
;             u32x4 bb[4][2]; f32x4 bf0[4][2], bf1[4][2];
; #pragma unroll
;             for (int m = 0; m < 4; ++m)
; #pragma unroll
;                 for (int bj = 0; bj < 2; ++bj) { const size_t off = (size_t)(row0 + ai * HALF + m * 16) * D + col0 + bj * HALF;
;                     if constexpr (BASE_F32) { bf0[m][bj] = *(const f32x4*)(basef + off); bf1[m][bj] = *(const f32x4*)(basef + off + 4); } else bb[m][bj] = *(const u32x4*)(hb + off); }
;             u32x2 p8[4][2];
; #pragma unroll
;             for (int m = 0; m < 4; ++m) {
;                 const int row = row0 + ai * HALF + m * 16; const size_t off = (size_t)row * D + col0; float ss = 0.f;
; #pragma unroll
;                 for (int bj = 0; bj < 2; ++bj) {
;                     f32x4 h0, h1;
;                     if constexpr (BASE_F32) { h0 = bf0[m][bj]; h1 = bf1[m][bj]; }
;                     else { const u32x4 b = bb[m][bj];
;                         h0 = (f32x4){__uint_as_float(b.x << 16), __uint_as_float(b.x & 0xffff0000u), __uint_as_float(b.y << 16), __uint_as_float(b.y & 0xffff0000u)};
;                         h1 = (f32x4){__uint_as_float(b.z << 16), __uint_as_float(b.z & 0xffff0000u), __uint_as_float(b.w << 16), __uint_as_float(b.w & 0xffff0000u)}; }
;                     h0 = h0 + acc[ai][bj][m][0]; h1 = h1 + acc[ai][bj][m][1];
;                     u32x4 w; w.x = cvt_pk_bf16(h0[0], h0[1]); w.y = cvt_pk_bf16(h0[2], h0[3]); w.z = cvt_pk_bf16(h1[0], h1[1]); w.w = cvt_pk_bf16(h1[2], h1[3]);
;                     if (WT && wt) st_wt16(hb + HO + off + bj * HALF, w); else *(u32x4*)(hb + HO + off + bj * HALF) = w;
.LBB0_891:
	v_mbcnt_lo_u32_b32 v130, -1, 0
	v_mbcnt_hi_u32_b32 v130, -1, v130
	s_lshl_b32 s4, s14, 8
	v_add_u32_e32 v130, s93, v130
	s_add_i32 s4, s4, s47
	v_and_b32_e32 v216, 15, v130
	v_or_b32_e32 v198, s4, v216
	s_lshl_b32 s4, s28, 8
	v_bfe_u32 v217, v130, 4, 2
	s_or_b32 s4, s4, s48
	v_lshl_or_b32 v196, v217, 3, s4
	v_ashrrev_i32_e32 v197, 31, v196
	v_ashrrev_i32_e32 v199, 31, v198
	v_lshl_add_u64 v[200:201], v[196:197], 2, s[2:3]
	v_lshlrev_b64 v[130:131], 12, v[198:199]
	v_or_b32_e32 v206, 16, v198
	v_lshl_add_u64 v[130:131], v[200:201], 0, v[130:131]
	v_ashrrev_i32_e32 v207, 31, v206
	global_load_dwordx4 v[222:225], v[130:131], off offset:16 nt
	global_load_dwordx4 v[210:213], v[130:131], off nt
	global_load_dwordx4 v[178:181], v[130:131], off offset:528 nt
	global_load_dwordx4 v[182:185], v[130:131], off offset:512 nt
	v_lshlrev_b64 v[130:131], 12, v[206:207]
	v_or_b32_e32 v204, 32, v198
	v_lshl_add_u64 v[130:131], v[200:201], 0, v[130:131]
	v_ashrrev_i32_e32 v205, 31, v204
	global_load_dwordx4 v[170:173], v[130:131], off offset:16 nt
	global_load_dwordx4 v[174:177], v[130:131], off nt
	global_load_dwordx4 v[162:165], v[130:131], off offset:528 nt
	global_load_dwordx4 v[166:169], v[130:131], off offset:512 nt
	v_lshlrev_b64 v[130:131], 12, v[204:205]
	v_or_b32_e32 v202, 48, v198
	v_lshl_add_u64 v[130:131], v[200:201], 0, v[130:131]
	v_ashrrev_i32_e32 v203, 31, v202
	global_load_dwordx4 v[154:157], v[130:131], off offset:16 nt
	global_load_dwordx4 v[158:161], v[130:131], off nt
	global_load_dwordx4 v[146:149], v[130:131], off offset:528 nt
	global_load_dwordx4 v[150:153], v[130:131], off offset:512 nt
	v_lshlrev_b64 v[130:131], 12, v[202:203]
	v_lshl_add_u64 v[134:135], v[200:201], 0, v[130:131]
	global_load_dwordx4 v[138:141], v[134:135], off offset:16 nt
	global_load_dwordx4 v[142:145], v[134:135], off nt
	global_load_dwordx4 v[130:133], v[134:135], off offset:528 nt
	s_nop 0
	global_load_dwordx4 v[134:137], v[134:135], off offset:512 nt
	v_lshlrev_b64 v[186:187], 11, v[198:199]
	v_lshl_add_u64 v[186:187], s[8:9], 0, v[186:187]
	s_and_b64 vcc, exec, s[12:13]
	s_mov_b64 s[76:77], 0x100
	s_waitcnt vmcnt(0)
	v_pk_add_f32 v[208:209], v[128:129], v[212:213]
	v_pk_add_f32 v[210:211], v[126:127], v[210:211]
	v_pk_add_f32 v[126:127], v[124:125], v[224:225]
	v_pk_add_f32 v[128:129], v[122:123], v[222:223]
	v_lshl_add_u64 v[212:213], v[196:197], 1, v[186:187]
	v_cvt_pk_bf16_f32 v122, v210, v211
	v_cvt_pk_bf16_f32 v123, v208, v209
	v_cvt_pk_bf16_f32 v124, v128, v129
	v_cvt_pk_bf16_f32 v125, v126, v127
	s_cbranch_vccz .LBB0_977
	global_store_dwordx4 v[212:213], v[122:125], off
	s_cbranch_execnz .LBB0_894

; __device__ __forceinline__ unsigned cvt_pk_bf16(float lo, float hi) { unsigned r; asm volatile("v_cvt_pk_bf16_f32 %0, %1, %2" : "=v"(r) : "v"(lo), "v"(hi)); return r; }
; __device__ __forceinline__ void st_wt16(void* p, u32x4 v) { asm volatile("global_store_dwordx4 %0, %1, off sc1\n\ts_nop 1" :: "v"(p), "v"(v) : "memory"); }
;     __device__ __forceinline__ void operator()(const f32x4 (&acc)[2][2][4][2], const Unit& u, int wr, int wc, int fr, int fq) const {
;     ...
;         for (int ai = 0; ai < 2; ++ai) {
;             u32x4 bb[4][2]; f32x4 bf0[4][2], bf1[4][2];
; #pragma unroll
;             for (int m = 0; m < 4; ++m)
; #pragma unroll
;                 for (int bj = 0; bj < 2; ++bj) { const size_t off = (size_t)(row0 + ai * HALF + m * 16) * D + col0 + bj * HALF;
;                     if constexpr (BASE_F32) { bf0[m][bj] = *(const f32x4*)(basef + off); bf1[m][bj] = *(const f32x4*)(basef + off + 4); } else bb[m][bj] = *(const u32x4*)(hb + off); }
;             u32x2 p8[4][2];
; #pragma unroll
;             for (int m = 0; m < 4; ++m) {
;                 const int row = row0 + ai * HALF + m * 16; const size_t off = (size_t)row * D + col0; float ss = 0.f;
; #pragma unroll
;                 for (int bj = 0; bj < 2; ++bj) {
;                     f32x4 h0, h1;
;                     if constexpr (BASE_F32) { h0 = bf0[m][bj]; h1 = bf1[m][bj]; }
;                     else { const u32x4 b = bb[m][bj];
;                         h0 = (f32x4){__uint_as_float(b.x << 16), __uint_as_float(b.x & 0xffff0000u), __uint_as_float(b.y << 16), __uint_as_float(b.y & 0xffff0000u)};
;                         h1 = (f32x4){__uint_as_float(b.z << 16), __uint_as_float(b.z & 0xffff0000u), __uint_as_float(b.w << 16), __uint_as_float(b.w & 0xffff0000u)}; }
;                     h0 = h0 + acc[ai][bj][m][0]; h1 = h1 + acc[ai][bj][m][1];
;                     u32x4 w; w.x = cvt_pk_bf16(h0[0], h0[1]); w.y = cvt_pk_bf16(h0[2], h0[3]); w.z = cvt_pk_bf16(h1[0], h1[1]); w.w = cvt_pk_bf16(h1[2], h1[3]);
;                     if (WT && wt) st_wt16(hb + HO + off + bj * HALF, w); else *(u32x4*)(hb + HO + off + bj * HALF) = w;
.LBB0_931:
	s_or_b64 exec, exec, s[30:31]
	v_add_u32_e32 v128, 0x80, v198
	v_ashrrev_i32_e32 v129, 31, v128
	v_lshlrev_b64 v[66:67], 12, v[128:129]
	v_add_u32_e32 v126, 0x90, v198
	v_lshl_add_u64 v[66:67], v[200:201], 0, v[66:67]
	v_ashrrev_i32_e32 v127, 31, v126
	global_load_dwordx4 v[134:137], v[66:67], off offset:16 nt
	global_load_dwordx4 v[138:141], v[66:67], off nt
	global_load_dwordx4 v[114:117], v[66:67], off offset:528 nt
	global_load_dwordx4 v[118:121], v[66:67], off offset:512 nt
	v_lshlrev_b64 v[66:67], 12, v[126:127]
	v_add_u32_e32 v124, 0xa0, v198
	v_lshl_add_u64 v[66:67], v[200:201], 0, v[66:67]
	v_ashrrev_i32_e32 v125, 31, v124
	global_load_dwordx4 v[106:109], v[66:67], off offset:16 nt
	global_load_dwordx4 v[110:113], v[66:67], off nt
	global_load_dwordx4 v[98:101], v[66:67], off offset:528 nt
	global_load_dwordx4 v[102:105], v[66:67], off offset:512 nt
	v_lshlrev_b64 v[66:67], 12, v[124:125]
	v_add_u32_e32 v122, 0xb0, v198
	v_lshl_add_u64 v[66:67], v[200:201], 0, v[66:67]
	v_ashrrev_i32_e32 v123, 31, v122
	global_load_dwordx4 v[90:93], v[66:67], off offset:16 nt
	global_load_dwordx4 v[94:97], v[66:67], off nt
	global_load_dwordx4 v[82:85], v[66:67], off offset:528 nt
	global_load_dwordx4 v[86:89], v[66:67], off offset:512 nt
	v_lshlrev_b64 v[66:67], 12, v[122:123]
	v_lshl_add_u64 v[70:71], v[200:201], 0, v[66:67]
	global_load_dwordx4 v[74:77], v[70:71], off offset:16 nt
	global_load_dwordx4 v[78:81], v[70:71], off nt
	global_load_dwordx4 v[66:69], v[70:71], off offset:528 nt
	s_nop 0
	global_load_dwordx4 v[70:73], v[70:71], off offset:512 nt
	s_and_b64 vcc, exec, s[4:5]
	s_waitcnt vmcnt(14)
	v_pk_add_f32 v[130:131], v[62:63], v[140:141]
	v_pk_add_f32 v[62:63], v[56:57], v[134:135]
	v_lshlrev_b64 v[134:135], 11, v[128:129]
	v_lshl_add_u64 v[134:135], s[8:9], 0, v[134:135]
	v_pk_add_f32 v[132:133], v[60:61], v[138:139]
	v_pk_add_f32 v[60:61], v[58:59], v[136:137]
	v_lshl_add_u64 v[134:135], v[196:197], 1, v[134:135]
	v_cvt_pk_bf16_f32 v56, v132, v133
	v_cvt_pk_bf16_f32 v57, v130, v131
	v_cvt_pk_bf16_f32 v58, v62, v63
	v_cvt_pk_bf16_f32 v59, v60, v61
	s_cbranch_vccnz .LBB0_985
	global_store_dwordx4 v[134:135], v[56:59], off
	s_cbranch_execnz .LBB0_934

; template <int PH, bool PRB = false>
; __device__ __forceinline__ void run_phase(int layer, LAS unsigned char* lds, const int wv_) {
;     ...
;                 if (layer == DEPTH - 1) {
;                     const float rs = rsqrtf(ss * (1.0f / D) + 1e-6f); float4* o4 = (float4*)(p.out + (size_t)r * D);
; #pragma unroll
;                     for (int j = 0; j < 4; ++j) { const float4 gg = gfin[j]; float4 o; o.x = v[j].x * rs * gg.x; o.y = v[j].y * rs * gg.y; o.z = v[j].z * rs * gg.z; o.w = v[j].w * rs * gg.w; o4[lane + 64 * j] = o; }
.LBB0_1851:
	s_and_b64 vcc, exec, s[20:21]
	s_cbranch_vccz .LBB0_1850
	v_cmp_gt_f32_e32 vcc, s61, v68
	s_nop 1
	v_cndmask_b32_e32 v56, v68, v69, vcc
	v_rsq_f32_e32 v68, v56
	v_lshl_add_u64 v[56:57], s[16:17], 0, v[64:65]
	v_mul_f32_e32 v69, 0x45800000, v68
	v_cndmask_b32_e32 v68, v68, v69, vcc
	v_pk_mul_f32 v[54:55], v[54:55], v[68:69] op_sel_hi:[1,0]
	v_pk_mul_f32 v[70:71], v[52:53], v[68:69] op_sel_hi:[1,0]
	v_pk_mul_f32 v[52:53], v[4:5], v[54:55]
	v_pk_mul_f32 v[54:55], v[6:7], v[70:71]
	v_pk_mul_f32 v[44:45], v[44:45], v[68:69] op_sel_hi:[1,0]
	v_pk_mul_f32 v[42:43], v[42:43], v[68:69] op_sel_hi:[1,0]
	v_pk_mul_f32 v[40:41], v[40:41], v[68:69] op_sel_hi:[1,0]
	global_store_dwordx4 v[56:57], v[52:55], off nt
	v_pk_mul_f32 v[42:43], v[12:13], v[42:43]
	v_pk_mul_f32 v[46:47], v[46:47], v[68:69] op_sel_hi:[1,0]
	v_pk_mul_f32 v[54:55], v[2:3], v[44:45]
	v_pk_mul_f32 v[44:45], v[14:15], v[40:41]
	global_store_dwordx4 v[56:57], v[42:45], off offset:2048 nt
	v_pk_mul_f32 v[40:41], v[48:49], v[68:69] op_sel_hi:[1,0]
	v_pk_mul_f32 v[52:53], v[0:1], v[46:47]
	v_pk_mul_f32 v[42:43], v[50:51], v[68:69] op_sel_hi:[1,0]
	v_pk_mul_f32 v[40:41], v[8:9], v[40:41]
	v_pk_mul_f32 v[42:43], v[10:11], v[42:43]
	global_store_dwordx4 v[56:57], v[52:55], off offset:1024 nt
	global_store_dwordx4 v[56:57], v[40:43], off offset:3072 nt
	s_andn2_b64 vcc, exec, s[18:19]
	s_cbranch_vccnz .LBB0_1843

; template <int PH, bool PRB = false>
; __device__ __forceinline__ void run_phase(int layer, LAS unsigned char* lds, const int wv_) {
;     ...
;                 if (layer == DEPTH - 1) {
;                     const float rs = rsqrtf(ss * (1.0f / D) + 1e-6f); float4* o4 = (float4*)(p.out + (size_t)r * D);
; #pragma unroll
;                     for (int j = 0; j < 4; ++j) { const float4 gg = gfin[j]; float4 o; o.x = v[j].x * rs * gg.x; o.y = v[j].y * rs * gg.y; o.z = v[j].z * rs * gg.z; o.w = v[j].w * rs * gg.w; o4[lane + 64 * j] = o; }
.LBB0_1859:
	s_and_b64 vcc, exec, s[18:19]
	s_cbranch_vccz .LBB0_1843
	v_cmp_gt_f32_e32 vcc, s61, v48
	s_nop 1
	v_cndmask_b32_e32 v48, v48, v49, vcc
	v_rsq_f32_e32 v50, v48
	v_lshl_add_u64 v[48:49], s[14:15], 0, v[64:65]
	v_mul_f32_e32 v51, 0x45800000, v50
	v_cndmask_b32_e32 v50, v50, v51, vcc
	v_pk_mul_f32 v[40:41], v[40:41], v[50:51] op_sel_hi:[1,0]
	v_pk_mul_f32 v[52:53], v[38:39], v[50:51] op_sel_hi:[1,0]
	v_pk_mul_f32 v[38:39], v[4:5], v[40:41]
	v_pk_mul_f32 v[40:41], v[6:7], v[52:53]
	global_store_dwordx4 v[48:49], v[38:41], off nt
	v_pk_mul_f32 v[36:37], v[36:37], v[50:51] op_sel_hi:[1,0]
	v_pk_mul_f32 v[34:35], v[34:35], v[50:51] op_sel_hi:[1,0]
	v_pk_mul_f32 v[38:39], v[42:43], v[50:51] op_sel_hi:[1,0]
	v_pk_mul_f32 v[40:41], v[2:3], v[36:37]
	v_pk_mul_f32 v[38:39], v[0:1], v[38:39]
	v_pk_mul_f32 v[36:37], v[44:45], v[50:51] op_sel_hi:[1,0]
	global_store_dwordx4 v[48:49], v[38:41], off offset:1024 nt
	v_pk_mul_f32 v[36:37], v[12:13], v[36:37]
	v_pk_mul_f32 v[32:33], v[32:33], v[50:51] op_sel_hi:[1,0]
	v_pk_mul_f32 v[38:39], v[14:15], v[34:35]
	v_pk_mul_f32 v[34:35], v[46:47], v[50:51] op_sel_hi:[1,0]
	global_store_dwordx4 v[48:49], v[36:39], off offset:2048 nt
	v_pk_mul_f32 v[34:35], v[8:9], v[34:35]
	s_nop 0
	v_pk_mul_f32 v[36:37], v[10:11], v[32:33]
	global_store_dwordx4 v[48:49], v[34:37], off offset:3072 nt
	s_branch .LBB0_1843
